# grid barrier: non-leader L1 invalidate issued before the release poll (overlapped with the wait) instead of after it, leader waits for its invalidate before releasing XGEN; spin loops poll without s_s
# speedup vs baseline: 1.0118x; 1.0118x over previous
.LBB0_88:
	s_or_b64 exec, exec, s[6:7]
	s_waitcnt vmcnt(0)
	buffer_inv sc1
	s_waitcnt vmcnt(0)
	global_atomic_add v[168:169], v1, off
	s_waitcnt vmcnt(0)

.LBB0_169:
	global_atomic_add v6, v[166:167], v1, off sc0
	v_cvt_f32_u32_e32 v2, v5
	v_sub_u32_e32 v7, 0, v5
	v_rcp_iflag_f32_e32 v2, v2
	s_nop 0
	v_mul_f32_e32 v2, 0x4f7ffffe, v2
	v_cvt_u32_f32_e32 v2, v2
	v_mul_lo_u32 v7, v7, v2
	v_mul_hi_u32 v7, v2, v7
	v_add_u32_e32 v2, v2, v7
	s_waitcnt vmcnt(0)
	v_mul_hi_u32 v2, v6, v2
	v_mul_lo_u32 v7, v2, v5
	v_sub_u32_e32 v7, v6, v7
	v_add_u32_e32 v8, 1, v2
	v_cmp_ge_u32_e32 vcc, v7, v5
	v_add_u32_e32 v6, 1, v6
	s_nop 0
	v_cndmask_b32_e32 v2, v2, v8, vcc
	v_sub_u32_e32 v8, v7, v5
	v_cndmask_b32_e32 v7, v7, v8, vcc
	v_add_u32_e32 v8, 1, v2
	v_cmp_ge_u32_e32 vcc, v7, v5
	s_nop 1
	v_cndmask_b32_e32 v2, v2, v8, vcc
	v_mul_lo_u32 v7, v5, v2
	v_add_u32_e32 v5, v7, v5
	v_cmp_ne_u32_e32 vcc, v6, v5
	s_and_saveexec_b64 s[4:5], vcc
	s_xor_b64 s[4:5], exec, s[4:5]
	s_cbranch_execz .LBB0_183
	s_waitcnt lgkmcnt(0)
	buffer_inv sc1
	global_load_dword v4, v[168:169], off sc1
	s_waitcnt vmcnt(0)
	v_cmp_eq_u32_e32 vcc, v4, v2
	s_and_saveexec_b64 s[6:7], vcc
	s_cbranch_execz .LBB0_182
	s_mov_b32 s22, 1
	s_mov_b64 s[8:9], 0
	s_branch .LBB0_173

.LBB0_182:
	s_or_b64 exec, exec, s[6:7]
	s_waitcnt vmcnt(0)
.LBB0_183:
	s_andn2_saveexec_b64 s[4:5], s[4:5]
	s_cbranch_execz .LBB0_201
	s_mov_b64 s[4:5], exec
	buffer_wbl2 sc1
	s_waitcnt lgkmcnt(0)
	s_waitcnt vmcnt(0)
	v_mbcnt_lo_u32_b32 v2, s4, 0
	v_mbcnt_hi_u32_b32 v2, s5, v2
	v_cmp_eq_u32_e32 vcc, 0, v2
	s_and_saveexec_b64 s[6:7], vcc
	s_cbranch_execz .LBB0_186
	s_bcnt1_i32_b64 s4, s[4:5]
	v_mov_b32_e32 v5, s4
	v_readlane_b32 s4, v249, 36
	v_readlane_b32 s5, v249, 37
	s_nop 4
	global_atomic_add v5, v3, v5, s[4:5] sc0

.LBB0_200:
	s_or_b64 exec, exec, s[4:5]
	s_waitcnt vmcnt(0)
	buffer_inv sc1
	s_waitcnt vmcnt(0)
	global_atomic_add v[168:169], v1, off
	s_waitcnt vmcnt(0)

.LBB0_309:
	s_or_b64 exec, exec, s[6:7]
	s_waitcnt vmcnt(0)
.LBB0_310:
	s_andn2_saveexec_b64 s[4:5], s[4:5]
	s_cbranch_execz .LBB0_328
	s_mov_b64 s[4:5], exec
	buffer_wbl2 sc1
	s_waitcnt lgkmcnt(0)
	s_waitcnt vmcnt(0)
	v_mbcnt_lo_u32_b32 v2, s4, 0
	v_mbcnt_hi_u32_b32 v2, s5, v2
	v_cmp_eq_u32_e32 vcc, 0, v2
	s_and_saveexec_b64 s[6:7], vcc
	s_cbranch_execz .LBB0_313
	s_bcnt1_i32_b64 s4, s[4:5]
	v_mov_b32_e32 v5, s4
	v_readlane_b32 s4, v249, 36
	v_readlane_b32 s5, v249, 37
	s_nop 4
	global_atomic_add v5, v3, v5, s[4:5] sc0

.LBB0_386:
	s_or_b64 exec, exec, s[6:7]
	s_waitcnt vmcnt(0)
.LBB0_387:
	s_andn2_saveexec_b64 s[4:5], s[4:5]
	s_cbranch_execz .LBB0_405
	s_mov_b64 s[4:5], exec
	buffer_wbl2 sc1
	s_waitcnt lgkmcnt(0)
	s_waitcnt vmcnt(0)
	v_mbcnt_lo_u32_b32 v2, s4, 0
	v_mbcnt_hi_u32_b32 v2, s5, v2
	v_cmp_eq_u32_e32 vcc, 0, v2
	s_and_saveexec_b64 s[6:7], vcc
	s_cbranch_execz .LBB0_390
	s_bcnt1_i32_b64 s4, s[4:5]
	v_mov_b32_e32 v5, s4
	v_readlane_b32 s4, v249, 36
	v_readlane_b32 s5, v249, 37
	s_nop 4
	global_atomic_add v5, v3, v5, s[4:5] sc0

.LBB0_448:
	s_or_b64 exec, exec, s[6:7]
	s_waitcnt vmcnt(0)
.LBB0_449:
	s_andn2_saveexec_b64 s[4:5], s[4:5]
	s_cbranch_execz .LBB0_467
	s_mov_b64 s[4:5], exec
	buffer_wbl2 sc1
	s_waitcnt lgkmcnt(0)
	s_waitcnt vmcnt(0)
	v_mbcnt_lo_u32_b32 v2, s4, 0
	v_mbcnt_hi_u32_b32 v2, s5, v2
	v_cmp_eq_u32_e32 vcc, 0, v2
	s_and_saveexec_b64 s[6:7], vcc
	s_cbranch_execz .LBB0_452
	s_bcnt1_i32_b64 s4, s[4:5]
	v_mov_b32_e32 v5, s4
	v_readlane_b32 s4, v249, 36
	v_readlane_b32 s5, v249, 37
	s_nop 4
	global_atomic_add v5, v3, v5, s[4:5] sc0

.LBB0_591:
	global_atomic_add v6, v[166:167], v1, off sc0
	v_cvt_f32_u32_e32 v2, v5
	v_sub_u32_e32 v7, 0, v5
	v_rcp_iflag_f32_e32 v2, v2
	s_nop 0
	v_mul_f32_e32 v2, 0x4f7ffffe, v2
	v_cvt_u32_f32_e32 v2, v2
	v_mul_lo_u32 v7, v7, v2
	v_mul_hi_u32 v7, v2, v7
	v_add_u32_e32 v2, v2, v7
	s_waitcnt vmcnt(0)
	v_mul_hi_u32 v2, v6, v2
	v_mul_lo_u32 v7, v2, v5
	v_sub_u32_e32 v7, v6, v7
	v_add_u32_e32 v8, 1, v2
	v_cmp_ge_u32_e32 vcc, v7, v5
	v_add_u32_e32 v6, 1, v6
	s_nop 0
	v_cndmask_b32_e32 v2, v2, v8, vcc
	v_sub_u32_e32 v8, v7, v5
	v_cndmask_b32_e32 v7, v7, v8, vcc
	v_add_u32_e32 v8, 1, v2
	v_cmp_ge_u32_e32 vcc, v7, v5
	s_nop 1
	v_cndmask_b32_e32 v2, v2, v8, vcc
	v_mul_lo_u32 v7, v5, v2
	v_add_u32_e32 v5, v7, v5
	v_cmp_ne_u32_e32 vcc, v6, v5
	s_and_saveexec_b64 s[6:7], vcc
	s_xor_b64 s[6:7], exec, s[6:7]
	s_cbranch_execz .LBB0_605
	s_waitcnt lgkmcnt(0)
	buffer_inv sc1
	global_load_dword v4, v[168:169], off sc1
	s_waitcnt vmcnt(0)
	v_cmp_eq_u32_e32 vcc, v4, v2
	s_and_saveexec_b64 s[8:9], vcc
	s_cbranch_execz .LBB0_604
	s_mov_b32 s22, 1
	s_mov_b64 s[10:11], 0
	s_branch .LBB0_595

.LBB0_604:
	s_or_b64 exec, exec, s[8:9]
	s_waitcnt vmcnt(0)
.LBB0_605:
	s_andn2_saveexec_b64 s[6:7], s[6:7]
	s_cbranch_execz .LBB0_623
	s_mov_b64 s[6:7], exec
	buffer_wbl2 sc1
	s_waitcnt lgkmcnt(0)
	s_waitcnt vmcnt(0)
	v_mbcnt_lo_u32_b32 v2, s6, 0
	v_mbcnt_hi_u32_b32 v2, s7, v2
	v_cmp_eq_u32_e32 vcc, 0, v2
	s_and_saveexec_b64 s[8:9], vcc
	s_cbranch_execz .LBB0_608
	s_bcnt1_i32_b64 s6, s[6:7]
	v_mov_b32_e32 v5, s6
	v_readlane_b32 s6, v249, 36
	v_readlane_b32 s7, v249, 37
	s_nop 4
	global_atomic_add v5, v3, v5, s[6:7] sc0

.LBB0_719:
	s_or_b64 exec, exec, s[6:7]
	s_waitcnt vmcnt(0)
.LBB0_720:
	s_andn2_saveexec_b64 s[4:5], s[4:5]
	s_cbranch_execz .LBB0_738
	s_mov_b64 s[4:5], exec
	buffer_wbl2 sc1
	s_waitcnt lgkmcnt(0)
	s_waitcnt vmcnt(0)
	v_mbcnt_lo_u32_b32 v2, s4, 0
	v_mbcnt_hi_u32_b32 v2, s5, v2
	v_cmp_eq_u32_e32 vcc, 0, v2
	s_and_saveexec_b64 s[6:7], vcc
	s_cbranch_execz .LBB0_723
	s_bcnt1_i32_b64 s4, s[4:5]
	v_mov_b32_e32 v5, s4
	v_readlane_b32 s4, v249, 36
	v_readlane_b32 s5, v249, 37
	s_nop 4
	global_atomic_add v5, v3, v5, s[4:5] sc0

.LBB0_774:
	s_or_b64 exec, exec, s[6:7]
	s_waitcnt vmcnt(0)
.LBB0_775:
	s_andn2_saveexec_b64 s[4:5], s[4:5]
	s_cbranch_execz .LBB0_793
	s_mov_b64 s[4:5], exec
	buffer_wbl2 sc1
	s_waitcnt lgkmcnt(0)
	s_waitcnt vmcnt(0)
	v_mbcnt_lo_u32_b32 v2, s4, 0
	v_mbcnt_hi_u32_b32 v2, s5, v2
	v_cmp_eq_u32_e32 vcc, 0, v2
	s_and_saveexec_b64 s[6:7], vcc
	s_cbranch_execz .LBB0_778
	s_bcnt1_i32_b64 s4, s[4:5]
	v_mov_b32_e32 v5, s4
	v_readlane_b32 s4, v249, 36
	v_readlane_b32 s5, v249, 37
	s_nop 4
	global_atomic_add v5, v3, v5, s[4:5] sc0

.LBB0_855:
	s_or_b64 exec, exec, s[6:7]
	s_waitcnt vmcnt(0)
.LBB0_856:
	s_andn2_saveexec_b64 s[4:5], s[4:5]
	s_cbranch_execz .LBB0_874
	s_mov_b64 s[4:5], exec
	buffer_wbl2 sc1
	s_waitcnt lgkmcnt(0)
	s_waitcnt vmcnt(0)
	v_mbcnt_lo_u32_b32 v2, s4, 0
	v_mbcnt_hi_u32_b32 v2, s5, v2
	v_cmp_eq_u32_e32 vcc, 0, v2
	s_and_saveexec_b64 s[6:7], vcc
	s_cbranch_execz .LBB0_859
	s_bcnt1_i32_b64 s4, s[4:5]
	v_mov_b32_e32 v5, s4
	v_readlane_b32 s4, v249, 36
	v_readlane_b32 s5, v249, 37
	s_nop 4
	global_atomic_add v5, v3, v5, s[4:5] sc0

.LBB0_958:
	s_or_b64 exec, exec, s[8:9]
	s_waitcnt vmcnt(0)
.LBB0_959:
	s_andn2_saveexec_b64 s[6:7], s[6:7]
	s_cbranch_execnz .LBB0_960
	s_getpc_b64 s[98:99]
